# one static priority raise for waves 4-7 over the attention and HGRN2 phases, reset before the next phase (on top of v21)
# speedup vs baseline: 1.0050x; 1.0050x over previous
.LBB0_1182:
	s_or_b64 exec, exec, s[6:7]
	v_readfirstlane_b32 s98, v0
	s_nop 3
	s_lshr_b32 s98, s98, 6
	s_cmp_ge_u32 s98, 4
	s_cbranch_scc0 .Lprio_p3
	s_setprio 1
.Lprio_p3:
	s_mov_b64 s[22:23], s[0:1]
	s_mov_b64 s[24:25], s[0:1]
	s_mov_b64 s[28:29], s[0:1]
	s_mov_b64 s[6:7], s[0:1]
	s_mov_b64 s[30:31], s[0:1]
	s_mov_b64 s[34:35], s[0:1]
	s_mov_b64 s[36:37], s[0:1]
	s_cmpk_gt_u32 s2, 0xff
	s_waitcnt lgkmcnt(0)
	s_barrier
	s_cbranch_scc1 .LBB0_1367
	s_load_dwordx2 s[6:7], s[6:7], 0x90
	s_lshr_b32 s8, s2, 4
	s_mov_b32 s9, 0
	v_mov_b32_e32 v21, v0
	s_lshl_b64 s[10:11], s[8:9], 15
	s_waitcnt lgkmcnt(0)
	s_barrier
	s_add_u32 s6, s6, s10
	v_lshlrev_b32_e32 v2, 4, v21
	s_addc_u32 s7, s7, s11
	v_ashrrev_i32_e32 v3, 31, v2
	v_lshl_add_u64 v[8:9], v[2:3], 2, s[6:7]
	s_mov_b32 s3, 0x1e300000
	v_add_co_u32_e32 v4, vcc, s3, v8
	s_mov_b64 s[6:7], 0x1e300000
	s_nop 0
	v_addc_co_u32_e32 v5, vcc, 0, v9, vcc
	global_load_dwordx4 v[4:7], v[4:5], off
	v_lshl_add_u64 v[12:13], v[8:9], 0, s[6:7]
	global_load_dwordx4 v[8:11], v[12:13], off offset:16
	global_load_dwordx4 v[26:29], v[12:13], off offset:32
	global_load_dwordx4 v[30:33], v[12:13], off offset:48
	v_mbcnt_hi_u32_b32 v23, -1, v1
	v_and_b32_e32 v24, 64, v23
	v_add_u32_e32 v3, -1, v23
	v_cmp_lt_i32_e32 vcc, v3, v24
	v_add_u32_e32 v20, -2, v23
	v_add_u32_e32 v25, -4, v23
	v_cndmask_b32_e32 v3, v3, v23, vcc
	v_lshlrev_b32_e32 v3, 2, v3
	v_cmp_lt_i32_e32 vcc, v20, v24
	v_cmp_lt_i32_e64 s[6:7], v25, v24
	s_waitcnt vmcnt(3)
	v_add_f32_e32 v18, 0, v4
	v_add_f32_e32 v19, v5, v18
	v_add_f32_e32 v16, v6, v19
	v_add_f32_e32 v17, v7, v16
	s_waitcnt vmcnt(2)
	v_add_f32_e32 v14, v8, v17
	v_add_f32_e32 v15, v9, v14
	v_add_f32_e32 v12, v10, v15
	v_add_f32_e32 v13, v11, v12
	s_waitcnt vmcnt(1)
	v_add_f32_e32 v10, v26, v13
	v_add_f32_e32 v11, v27, v10
	v_add_f32_e32 v8, v28, v11
	v_add_f32_e32 v9, v29, v8
	s_waitcnt vmcnt(0)
	v_add_f32_e32 v6, v30, v9
	v_add_f32_e32 v7, v31, v6
	v_add_f32_e32 v4, v32, v7
	v_add_f32_e32 v5, v33, v4
	ds_bpermute_b32 v22, v3, v5
	v_and_b32_e32 v3, 63, v21
	v_cndmask_b32_e32 v20, v20, v23, vcc
	v_cmp_eq_u32_e32 vcc, 0, v3
	v_lshlrev_b32_e32 v20, 2, v20
	s_waitcnt lgkmcnt(0)
	v_add_f32_e32 v22, v5, v22
	v_cndmask_b32_e32 v22, v22, v5, vcc
	ds_bpermute_b32 v20, v20, v22
	v_cndmask_b32_e64 v25, v25, v23, s[6:7]
	v_cmp_gt_u32_e64 s[6:7], 2, v3
	v_lshlrev_b32_e32 v25, 2, v25
	v_ashrrev_i32_e32 v26, 6, v21
	s_waitcnt lgkmcnt(0)
	v_add_f32_e32 v20, v22, v20
	v_cndmask_b32_e64 v20, v20, v22, s[6:7]
	ds_bpermute_b32 v22, v25, v20
	v_add_u32_e32 v25, -8, v23
	v_cmp_lt_i32_e64 s[6:7], v25, v24
	s_waitcnt lgkmcnt(0)
	v_add_f32_e32 v22, v20, v22
	v_cndmask_b32_e64 v25, v25, v23, s[6:7]
	v_cmp_gt_u32_e64 s[6:7], 4, v3
	v_lshlrev_b32_e32 v25, 2, v25
	s_nop 0
	v_cndmask_b32_e64 v20, v22, v20, s[6:7]
	ds_bpermute_b32 v22, v25, v20
	v_add_u32_e32 v25, -16, v23
	v_cmp_lt_i32_e64 s[6:7], v25, v24
	s_waitcnt lgkmcnt(0)
	v_add_f32_e32 v22, v20, v22
	v_cndmask_b32_e64 v25, v25, v23, s[6:7]
	v_cmp_gt_u32_e64 s[6:7], 8, v3
	v_lshlrev_b32_e32 v25, 2, v25
	s_nop 0
	v_cndmask_b32_e64 v20, v22, v20, s[6:7]
	ds_bpermute_b32 v22, v25, v20
	v_subrev_u32_e32 v25, 32, v23
	v_cmp_lt_i32_e64 s[6:7], v25, v24
	s_waitcnt lgkmcnt(0)
	v_add_f32_e32 v22, v20, v22
	v_cndmask_b32_e64 v25, v25, v23, s[6:7]
	v_cmp_gt_u32_e64 s[6:7], 16, v3
	v_lshlrev_b32_e32 v25, 2, v25
	s_nop 0
	v_cndmask_b32_e64 v20, v22, v20, s[6:7]
	ds_bpermute_b32 v22, v25, v20
	v_cmp_eq_u32_e64 s[6:7], 63, v3
	s_waitcnt lgkmcnt(0)
	v_add_f32_e32 v25, v20, v22
	v_lshl_add_u32 v22, v26, 2, 0
	s_and_saveexec_b64 s[10:11], s[6:7]
	v_add_u32_e32 v27, 0x10000, v22
	ds_write_b32 v27, v25
	s_or_b64 exec, exec, s[10:11]
	s_load_dwordx2 s[16:17], s[22:23], 0x90
	s_load_dwordx2 s[12:13], s[24:25], 0x90
	s_load_dwordx2 s[14:15], s[28:29], 0x90
	s_load_dwordx2 s[20:21], s[36:37], 0x90
	s_load_dwordx2 s[18:19], s[30:31], 0x40
	s_load_dwordx2 s[10:11], s[34:35], 0x48
	v_cmp_gt_u32_e64 s[6:7], 32, v3
	s_waitcnt lgkmcnt(0)
	s_barrier
	v_cndmask_b32_e64 v20, v25, v20, s[6:7]
	v_sub_f32_e32 v20, v20, v5
	v_cmp_lt_i32_e64 s[6:7], 0, v26
	s_and_saveexec_b64 s[22:23], s[6:7]
	s_cbranch_execz .LBB0_1195
	v_cmp_lt_u32_e64 s[6:7], 7, v26
	v_mov_b32_e32 v25, 0
	s_and_saveexec_b64 s[24:25], s[6:7]
	s_cbranch_execz .LBB0_1190
	s_mov_b32 s3, 0
	s_add_i32 s30, 0, 0x10000
	v_and_b32_e32 v25, 0x7ffffff8, v26
	s_mov_b64 s[28:29], 0

.LBB0_1472:
	s_setprio 0
	s_waitcnt vmcnt(0)
	s_barrier
	s_and_saveexec_b64 s[8:9], s[4:5]
	s_cbranch_execz .LBB0_1524
	s_add_i32 s3, 0, 0x24020
	v_mov_b32_e32 v2, s3
	s_waitcnt vmcnt(0) expcnt(0) lgkmcnt(0)
	ds_read_b32 v4, v2
	s_add_i32 s3, 0, 0x24024
	v_mov_b32_e32 v2, s3
	ds_read_b32 v2, v2
	s_waitcnt lgkmcnt(1)
	v_cmp_ne_u32_e32 vcc, 0, v4
	s_cbranch_vccnz .LBB0_1488
	s_load_dwordx2 s[14:15], s[48:49], 0x4
	s_add_u32 s10, s44, 0x1000
	s_addc_u32 s11, s45, 0
	s_add_u32 s12, s44, 0x1100
	s_addc_u32 s13, s45, 0
	s_waitcnt lgkmcnt(0)
	s_mul_i32 s3, s14, s46
	s_add_u32 s14, s44, 0x1200
	s_mul_i32 s3, s3, s15
	s_addc_u32 s15, s45, 0
	s_add_u32 s16, s44, 0x1300
	s_addc_u32 s17, s45, 0
	s_mov_b32 s24, 1
	v_mov_b32_e32 v18, 0
	s_branch .LBB0_1476
